# chunk-to-wave remap: rank the 8 per-wave edge loads, SIMD pair (w,w+4) gets lightest+heaviest
# speedup vs baseline: 1.0090x; 1.0078x over previous
.LBB1_141:
	s_or_b64 exec, exec, s[6:7]
	v_and_b32_e32 v1, 31, v0
	s_waitcnt lgkmcnt(0)
	v_lshlrev_b32_e32 v2, 2, v1
	v_or_b32_e32 v22, 32, v8
	s_barrier
	v_readfirstlane_b32 s95, v9
	v_min_u32_e32 v24, 8, v1
	v_mov_b32_e32 v25, 0x12810
	v_lshl_add_u32 v25, v24, 10, v25
	ds_read_b32 v25, v25
	v_mov_b32_e32 v27, 0
	s_waitcnt lgkmcnt(0)
	v_mov_b32_e32 v26, v25
	s_nop 1
	v_mov_b32_dpp v26, v25 row_shl:1 row_mask:0xf bank_mask:0xf
	v_sub_u32_e32 v26, v26, v25
	v_lshl_or_b32 v26, v26, 3, v24
	s_nop 1
	v_readlane_b32 s86, v26, 0
	v_readlane_b32 s87, v26, 1
	v_readlane_b32 s88, v26, 2
	v_readlane_b32 s89, v26, 3
	v_readlane_b32 s90, v26, 4
	v_readlane_b32 s91, v26, 5
	v_readlane_b32 s92, v26, 6
	v_readlane_b32 s93, v26, 7
	v_cmp_lt_u32_e32 vcc, s86, v26
	v_addc_co_u32_e32 v27, vcc, 0, v27, vcc
	v_cmp_lt_u32_e32 vcc, s87, v26
	v_addc_co_u32_e32 v27, vcc, 0, v27, vcc
	v_cmp_lt_u32_e32 vcc, s88, v26
	v_addc_co_u32_e32 v27, vcc, 0, v27, vcc
	v_cmp_lt_u32_e32 vcc, s89, v26
	v_addc_co_u32_e32 v27, vcc, 0, v27, vcc
	v_cmp_lt_u32_e32 vcc, s90, v26
	v_addc_co_u32_e32 v27, vcc, 0, v27, vcc
	v_cmp_lt_u32_e32 vcc, s91, v26
	v_addc_co_u32_e32 v27, vcc, 0, v27, vcc
	v_cmp_lt_u32_e32 vcc, s92, v26
	v_addc_co_u32_e32 v27, vcc, 0, v27, vcc
	v_cmp_lt_u32_e32 vcc, s93, v26
	v_addc_co_u32_e32 v27, vcc, 0, v27, vcc
	v_sub_u32_e32 v24, 11, v27
	v_cmp_gt_u32_e32 vcc, 4, v27
	v_cndmask_b32_e32 v27, v24, v27, vcc
	v_cmp_eq_u32_e32 vcc, s95, v27
	s_ff1_i32_b64 s95, vcc
	v_mov_b32_e32 v9, s95
	s_lshl_b32 s84, s95, 3
	s_add_u32 s85, s84, 8
	v_lshlrev_b32_e32 v3, 2, v22
	s_waitcnt vmcnt(0)
	v_mov_b32_e32 v18, v108
	v_mov_b32_e32 v19, v109
	v_mov_b32_e32 v20, v110
	v_mov_b32_e32 v16, v111
	v_mov_b32_e32 v17, v112
	v_mov_b32_e32 v12, v113
	v_mov_b32_e32 v13, v114
	v_mov_b32_e32 v15, v115
	v_mov_b32_e32 v4, 0x180
	v_lshl_or_b32 v23, v8, 2, v4
	v_mov_b32_e32 v21, v116
	v_mov_b32_e32 v4, v117
	v_mov_b32_e32 v5, v118
	v_mov_b32_e32 v10, v119
	v_mov_b32_e32 v3, 0x12810
	v_lshl_add_u32 v23, v9, 10, v3
	ds_read2_b32 v[24:25], v23 offset1:32
	v_add_u32_e32 v2, v23, v2
	ds_read2_b32 v[230:231], v2 offset1:1
	v_lshlrev_b32_e32 v26, 8, v9
	s_lshl_b32 s2, s2, 11
	v_or3_b32 v235, v26, s2, v1
	s_mov_b32 s12, 0x7a120
	s_waitcnt lgkmcnt(1)
	v_readfirstlane_b32 s13, v24
	v_readfirstlane_b32 s6, v25
	v_cmp_gt_i32_e32 vcc, s12, v235
	v_mov_b32_e32 v2, 0
	v_mov_b32_e32 v238, 0
	s_and_saveexec_b64 s[2:3], vcc
	s_cbranch_execz .LBB1_143
	v_ashrrev_i32_e32 v25, 31, v235
	v_mov_b32_e32 v24, v235
	v_lshl_add_u64 v[24:25], v[24:25], 2, s[50:51]
	global_load_dword v238, v[24:25], off
